# in-proj GEMM epilogue: bf16 output rows pass through a private per-wave LDS image so each global_store_dwordx4 writes 8 full 128-byte lines instead of 64 scattered 16-byte pieces
# speedup vs baseline: 1.0157x; 1.0071x over previous
; #define LAS __attribute__((address_space(3)))
; __device__ __forceinline__ unsigned cvt_pk_bf16(float lo, float hi) { unsigned r; asm volatile("v_cvt_pk_bf16_f32 %0, %1, %2" : "=v"(r) : "v"(lo), "v"(hi)); return r; }
;     __device__ __forceinline__ void operator()(const f32x4 (&acc)[2][2][4][2], const Unit& u, int wr, int wc, int fr, int fq, const LAS unsigned* rt) const {
;         const float sc = INV_IN8 * ((u.pn < 2) ? 0.125f : ((u.pn == 8 || u.pn == 9) ? 0.08838834764831845f : 1.f));
;         const int row0 = u.pm * BM + wr * 64 + fr, col0 = u.pn * BM + wc * 64 + 16 * fq;
; #pragma unroll
;         for (int ai = 0; ai < 2; ++ai)
; #pragma unroll
;             for (int m = 0; m < 4; ++m) { bf16_t* rowp = O + (size_t)(row0 + ai * HALF + m * 16) * DIN + col0;
; #pragma unroll
;                 for (int bj = 0; bj < 2; ++bj) { const f32x4 v0 = acc[ai][bj][m][0] * sc, v1 = acc[ai][bj][m][1] * sc;
;                     u32x4 w; w.x = cvt_pk_bf16(v0[0], v0[1]); w.y = cvt_pk_bf16(v0[2], v0[3]); w.z = cvt_pk_bf16(v1[0], v1[1]); w.w = cvt_pk_bf16(v1[2], v1[3]);
;                     *(u32x4*)(rowp + 8 * bj) = w; } }
;     }
.LBB0_210:
	s_and_b32 s4, s52, -2
	s_cmp_eq_u32 s4, 8
	s_cselect_b64 vcc, -1, 0
	s_cmp_gt_i32 s52, 1
	v_mbcnt_lo_u32_b32 v16, -1, 0
	v_mbcnt_hi_u32_b32 v16, -1, v16
	v_and_b32_e32 v17, 7, v16
	v_lshrrev_b32_e32 v18, 3, v16
	v_and_b32_e32 v26, 0xffffffc0, v184
	v_lshl_or_b32 v26, v17, 3, v26
	v_and_b32_e32 v27, 0xffffffc0, v183
	v_or_b32_e32 v27, v27, v18
	v_lshrrev_b32_e32 v19, 6, v183
	v_lshrrev_b32_e32 v21, 6, v184
	v_lshl_add_u32 v19, v19, 2, v21
	v_mul_u32_u24_e32 v19, 0x900, v19
	v_add_u32_e32 v19, 0x20000, v19
	v_and_b32_e32 v21, 15, v183
	v_mul_u32_u24_e32 v21, 0x90, v21
	v_bfe_u32 v23, v184, 4, 2
	v_lshl_add_u32 v21, v23, 5, v21
	v_add_u32_e32 v21, v21, v19
	v_mul_u32_u24_e32 v23, 0x90, v18
	v_lshl_add_u32 v23, v17, 4, v23
	v_add_u32_e32 v23, v23, v19
	v_mov_b32_e32 v16, 0xe000
	v_mov_b32_e32 v17, 0
	v_lshl_add_u32 v4, s52, 8, v26
	v_cndmask_b32_e32 v0, v186, v187, vcc
	s_cselect_b64 vcc, -1, 0
	v_lshl_add_u32 v1, s28, 8, v27
	v_ashrrev_i32_e32 v5, 31, v4
	v_mov_b64_e32 v[2:3], s[16:17]
	v_cndmask_b32_e32 v0, v188, v0, vcc
	v_mad_i64_i32 v[6:7], s[4:5], v1, s51, v[2:3]
	v_lshlrev_b64 v[4:5], 1, v[4:5]
	s_nop 15
	s_nop 15
	v_lshl_add_u64 v[10:11], v[6:7], 0, v[4:5]
	v_pk_mul_f32 v[6:7], v[0:1], v[152:153] op_sel_hi:[0,1]
	v_pk_mul_f32 v[8:9], v[0:1], v[154:155] op_sel_hi:[0,1]
	v_cvt_pk_bf16_f32 v6, v6, v7
	v_cvt_pk_bf16_f32 v7, v8, v9
	v_pk_mul_f32 v[12:13], v[0:1], v[150:151] op_sel_hi:[0,1]
	v_pk_mul_f32 v[14:15], v[0:1], v[148:149] op_sel_hi:[0,1]
	v_cvt_pk_bf16_f32 v8, v14, v15
	v_cvt_pk_bf16_f32 v9, v12, v13
	v_mov_b64_e32 v[204:205], v[10:11]
	v_lshl_add_u64 v[208:209], v[10:11], 0, v[16:17]
	ds_write_b128 v21, v[6:9]
	v_pk_mul_f32 v[12:13], v[0:1], v[142:143] op_sel_hi:[0,1]
	v_pk_mul_f32 v[14:15], v[0:1], v[140:141] op_sel_hi:[0,1]
	v_pk_mul_f32 v[6:7], v[0:1], v[144:145] op_sel_hi:[0,1]
	v_pk_mul_f32 v[8:9], v[0:1], v[146:147] op_sel_hi:[0,1]
	v_cvt_pk_bf16_f32 v6, v6, v7
	v_cvt_pk_bf16_f32 v7, v8, v9
	v_cvt_pk_bf16_f32 v8, v14, v15
	v_cvt_pk_bf16_f32 v9, v12, v13
	ds_write_b128 v21, v[6:9] offset:16
	ds_read_b128 v[192:195], v23
	ds_read_b128 v[196:199], v23 offset:1152
	v_pk_mul_f32 v[12:13], v[0:1], v[134:135] op_sel_hi:[0,1]
	v_pk_mul_f32 v[14:15], v[0:1], v[132:133] op_sel_hi:[0,1]
	v_or_b32_e32 v6, 16, v1
	v_mad_i64_i32 v[6:7], s[4:5], v6, s51, v[2:3]
	v_lshl_add_u64 v[10:11], v[6:7], 0, v[4:5]
	v_pk_mul_f32 v[6:7], v[0:1], v[136:137] op_sel_hi:[0,1]
	v_pk_mul_f32 v[8:9], v[0:1], v[138:139] op_sel_hi:[0,1]
	v_cvt_pk_bf16_f32 v6, v6, v7
	v_cvt_pk_bf16_f32 v7, v8, v9
	v_cvt_pk_bf16_f32 v8, v14, v15
	v_cvt_pk_bf16_f32 v9, v12, v13
	v_mov_b64_e32 v[206:207], v[10:11]
	v_lshl_add_u64 v[210:211], v[10:11], 0, v[16:17]
	ds_write_b128 v21, v[6:9]
	v_pk_mul_f32 v[12:13], v[0:1], v[126:127] op_sel_hi:[0,1]
	v_pk_mul_f32 v[14:15], v[0:1], v[124:125] op_sel_hi:[0,1]
	v_pk_mul_f32 v[6:7], v[0:1], v[128:129] op_sel_hi:[0,1]
	v_pk_mul_f32 v[8:9], v[0:1], v[130:131] op_sel_hi:[0,1]
	v_cvt_pk_bf16_f32 v6, v6, v7
	v_cvt_pk_bf16_f32 v7, v8, v9
	v_cvt_pk_bf16_f32 v8, v14, v15
	v_cvt_pk_bf16_f32 v9, v12, v13
	s_waitcnt lgkmcnt(1)
	global_store_dwordx4 v[204:205], v[192:195], off
	global_store_dwordx4 v[208:209], v[196:199], off
	ds_write_b128 v21, v[6:9] offset:16
	ds_read_b128 v[192:195], v23
	ds_read_b128 v[196:199], v23 offset:1152
	v_pk_mul_f32 v[12:13], v[0:1], v[118:119] op_sel_hi:[0,1]
	v_pk_mul_f32 v[14:15], v[0:1], v[116:117] op_sel_hi:[0,1]
	v_or_b32_e32 v6, 32, v1
	v_mad_i64_i32 v[6:7], s[4:5], v6, s51, v[2:3]
	v_lshl_add_u64 v[10:11], v[6:7], 0, v[4:5]
	v_pk_mul_f32 v[6:7], v[0:1], v[120:121] op_sel_hi:[0,1]
	v_pk_mul_f32 v[8:9], v[0:1], v[122:123] op_sel_hi:[0,1]
	v_cvt_pk_bf16_f32 v6, v6, v7
	v_cvt_pk_bf16_f32 v7, v8, v9
	v_cvt_pk_bf16_f32 v8, v14, v15
	v_cvt_pk_bf16_f32 v9, v12, v13
	v_mov_b64_e32 v[204:205], v[10:11]
	v_lshl_add_u64 v[208:209], v[10:11], 0, v[16:17]
	ds_write_b128 v21, v[6:9]
	v_pk_mul_f32 v[12:13], v[0:1], v[110:111] op_sel_hi:[0,1]
	v_pk_mul_f32 v[14:15], v[0:1], v[108:109] op_sel_hi:[0,1]
	v_pk_mul_f32 v[6:7], v[0:1], v[112:113] op_sel_hi:[0,1]
	v_pk_mul_f32 v[8:9], v[0:1], v[114:115] op_sel_hi:[0,1]
	v_cvt_pk_bf16_f32 v6, v6, v7
	v_cvt_pk_bf16_f32 v7, v8, v9
	v_cvt_pk_bf16_f32 v8, v14, v15
	v_cvt_pk_bf16_f32 v9, v12, v13
	s_waitcnt lgkmcnt(1)
	global_store_dwordx4 v[206:207], v[192:195], off
	global_store_dwordx4 v[210:211], v[196:199], off
	ds_write_b128 v21, v[6:9] offset:16
	ds_read_b128 v[192:195], v23
	ds_read_b128 v[196:199], v23 offset:1152
	v_pk_mul_f32 v[12:13], v[0:1], v[98:99] op_sel_hi:[0,1]
	v_pk_mul_f32 v[14:15], v[0:1], v[96:97] op_sel_hi:[0,1]
	v_or_b32_e32 v6, 48, v1
	v_mad_i64_i32 v[6:7], s[4:5], v6, s51, v[2:3]
	v_lshl_add_u64 v[10:11], v[6:7], 0, v[4:5]
	v_pk_mul_f32 v[6:7], v[0:1], v[104:105] op_sel_hi:[0,1]
	v_pk_mul_f32 v[8:9], v[0:1], v[106:107] op_sel_hi:[0,1]
	v_cvt_pk_bf16_f32 v6, v6, v7
	v_cvt_pk_bf16_f32 v7, v8, v9
	v_cvt_pk_bf16_f32 v8, v14, v15
	v_cvt_pk_bf16_f32 v9, v12, v13
	v_mov_b64_e32 v[206:207], v[10:11]
	v_lshl_add_u64 v[210:211], v[10:11], 0, v[16:17]
	ds_write_b128 v21, v[6:9]
	v_pk_mul_f32 v[12:13], v[0:1], v[90:91] op_sel_hi:[0,1]
	v_pk_mul_f32 v[14:15], v[0:1], v[88:89] op_sel_hi:[0,1]
	v_pk_mul_f32 v[6:7], v[0:1], v[92:93] op_sel_hi:[0,1]
	v_pk_mul_f32 v[8:9], v[0:1], v[94:95] op_sel_hi:[0,1]
	v_cvt_pk_bf16_f32 v6, v6, v7
	v_cvt_pk_bf16_f32 v7, v8, v9
	v_cvt_pk_bf16_f32 v8, v14, v15
	v_cvt_pk_bf16_f32 v9, v12, v13
	s_waitcnt lgkmcnt(1)
; __device__ __forceinline__ unsigned cvt_pk_bf16(float lo, float hi) { unsigned r; asm volatile("v_cvt_pk_bf16_f32 %0, %1, %2" : "=v"(r) : "v"(lo), "v"(hi)); return r; }
;     __device__ __forceinline__ void operator()(const f32x4 (&acc)[2][2][4][2], const Unit& u, int wr, int wc, int fr, int fq, const LAS unsigned* rt) const {
;     ...
; #pragma unroll
;         for (int ai = 0; ai < 2; ++ai)
; #pragma unroll
;             for (int m = 0; m < 4; ++m) { bf16_t* rowp = O + (size_t)(row0 + ai * HALF + m * 16) * DIN + col0;
; #pragma unroll
;                 for (int bj = 0; bj < 2; ++bj) { const f32x4 v0 = acc[ai][bj][m][0] * sc, v1 = acc[ai][bj][m][1] * sc;
;                     u32x4 w; w.x = cvt_pk_bf16(v0[0], v0[1]); w.y = cvt_pk_bf16(v0[2], v0[3]); w.z = cvt_pk_bf16(v1[0], v1[1]); w.w = cvt_pk_bf16(v1[2], v1[3]);
;                     *(u32x4*)(rowp + 8 * bj) = w; } }
;     }
	global_store_dwordx4 v[204:205], v[192:195], off
	global_store_dwordx4 v[208:209], v[196:199], off
	ds_write_b128 v21, v[6:9] offset:16
	ds_read_b128 v[192:195], v23
	ds_read_b128 v[196:199], v23 offset:1152
	v_pk_mul_f32 v[12:13], v[0:1], v[82:83] op_sel_hi:[0,1]
	v_pk_mul_f32 v[14:15], v[0:1], v[80:81] op_sel_hi:[0,1]
	v_add_u32_e32 v6, 0x80, v1
	v_mad_i64_i32 v[6:7], s[4:5], v6, s51, v[2:3]
	v_lshl_add_u64 v[10:11], v[6:7], 0, v[4:5]
	v_pk_mul_f32 v[6:7], v[0:1], v[84:85] op_sel_hi:[0,1]
	v_pk_mul_f32 v[8:9], v[0:1], v[86:87] op_sel_hi:[0,1]
	v_cvt_pk_bf16_f32 v6, v6, v7
	v_cvt_pk_bf16_f32 v7, v8, v9
	v_cvt_pk_bf16_f32 v8, v14, v15
	v_cvt_pk_bf16_f32 v9, v12, v13
	v_mov_b64_e32 v[204:205], v[10:11]
	v_lshl_add_u64 v[208:209], v[10:11], 0, v[16:17]
	ds_write_b128 v21, v[6:9]
	v_pk_mul_f32 v[12:13], v[0:1], v[102:103] op_sel_hi:[0,1]
	v_pk_mul_f32 v[14:15], v[0:1], v[100:101] op_sel_hi:[0,1]
	v_pk_mul_f32 v[6:7], v[0:1], v[76:77] op_sel_hi:[0,1]
	v_pk_mul_f32 v[8:9], v[0:1], v[78:79] op_sel_hi:[0,1]
	v_cvt_pk_bf16_f32 v6, v6, v7
	v_cvt_pk_bf16_f32 v7, v8, v9
	v_cvt_pk_bf16_f32 v8, v14, v15
	v_cvt_pk_bf16_f32 v9, v12, v13
	s_waitcnt lgkmcnt(1)
	global_store_dwordx4 v[206:207], v[192:195], off
	global_store_dwordx4 v[210:211], v[196:199], off
	ds_write_b128 v21, v[6:9] offset:16
	ds_read_b128 v[192:195], v23
	ds_read_b128 v[196:199], v23 offset:1152
	v_pk_mul_f32 v[12:13], v[0:1], v[62:63] op_sel_hi:[0,1]
	v_pk_mul_f32 v[14:15], v[0:1], v[60:61] op_sel_hi:[0,1]
	v_add_u32_e32 v6, 0x90, v1
	v_mad_i64_i32 v[6:7], s[4:5], v6, s51, v[2:3]
	v_lshl_add_u64 v[10:11], v[6:7], 0, v[4:5]
	v_pk_mul_f32 v[6:7], v[0:1], v[64:65] op_sel_hi:[0,1]
	v_pk_mul_f32 v[8:9], v[0:1], v[66:67] op_sel_hi:[0,1]
	v_cvt_pk_bf16_f32 v6, v6, v7
	v_cvt_pk_bf16_f32 v7, v8, v9
	v_cvt_pk_bf16_f32 v8, v14, v15
	v_cvt_pk_bf16_f32 v9, v12, v13
	v_mov_b64_e32 v[206:207], v[10:11]
	v_lshl_add_u64 v[210:211], v[10:11], 0, v[16:17]
	ds_write_b128 v21, v[6:9]
	v_pk_mul_f32 v[12:13], v[0:1], v[70:71] op_sel_hi:[0,1]
	v_pk_mul_f32 v[14:15], v[0:1], v[68:69] op_sel_hi:[0,1]
	v_pk_mul_f32 v[6:7], v[0:1], v[72:73] op_sel_hi:[0,1]
	v_pk_mul_f32 v[8:9], v[0:1], v[74:75] op_sel_hi:[0,1]
	v_cvt_pk_bf16_f32 v6, v6, v7
	v_cvt_pk_bf16_f32 v7, v8, v9
	v_cvt_pk_bf16_f32 v8, v14, v15
	v_cvt_pk_bf16_f32 v9, v12, v13
	s_waitcnt lgkmcnt(1)
	global_store_dwordx4 v[204:205], v[192:195], off
	global_store_dwordx4 v[208:209], v[196:199], off
	ds_write_b128 v21, v[6:9] offset:16
	ds_read_b128 v[192:195], v23
	ds_read_b128 v[196:199], v23 offset:1152
	v_pk_mul_f32 v[12:13], v[0:1], v[46:47] op_sel_hi:[0,1]
	v_pk_mul_f32 v[14:15], v[0:1], v[44:45] op_sel_hi:[0,1]
	v_add_u32_e32 v6, 0xa0, v1
	v_mad_i64_i32 v[6:7], s[4:5], v6, s51, v[2:3]
	v_lshl_add_u64 v[10:11], v[6:7], 0, v[4:5]
	v_pk_mul_f32 v[8:9], v[0:1], v[50:51] op_sel_hi:[0,1]
	v_pk_mul_f32 v[6:7], v[0:1], v[48:49] op_sel_hi:[0,1]
	v_cvt_pk_bf16_f32 v6, v6, v7
	v_cvt_pk_bf16_f32 v7, v8, v9
	v_cvt_pk_bf16_f32 v8, v14, v15
	v_cvt_pk_bf16_f32 v9, v12, v13
	v_mov_b64_e32 v[204:205], v[10:11]
	v_lshl_add_u64 v[208:209], v[10:11], 0, v[16:17]
	ds_write_b128 v21, v[6:9]
	v_pk_mul_f32 v[12:13], v[0:1], v[54:55] op_sel_hi:[0,1]
	v_pk_mul_f32 v[14:15], v[0:1], v[52:53] op_sel_hi:[0,1]
	v_pk_mul_f32 v[8:9], v[0:1], v[58:59] op_sel_hi:[0,1]
	v_pk_mul_f32 v[6:7], v[0:1], v[56:57] op_sel_hi:[0,1]
	v_add_u32_e32 v1, 0xb0, v1
	v_cvt_pk_bf16_f32 v6, v6, v7
	v_cvt_pk_bf16_f32 v7, v8, v9
	v_mad_i64_i32 v[2:3], s[4:5], v1, s51, v[2:3]
	v_cvt_pk_bf16_f32 v8, v14, v15
	v_cvt_pk_bf16_f32 v9, v12, v13
	s_waitcnt lgkmcnt(1)
	global_store_dwordx4 v[206:207], v[192:195], off
	global_store_dwordx4 v[210:211], v[196:199], off
	ds_write_b128 v21, v[6:9] offset:16
	ds_read_b128 v[192:195], v23
	ds_read_b128 v[196:199], v23 offset:1152
	v_pk_mul_f32 v[10:11], v[0:1], v[32:33] op_sel_hi:[0,1]
	s_andn2_b64 vcc, exec, s[6:7]
	v_lshl_add_u64 v[6:7], v[2:3], 0, v[4:5]
	v_pk_mul_f32 v[2:3], v[0:1], v[36:37] op_sel_hi:[0,1]
	v_pk_mul_f32 v[4:5], v[0:1], v[38:39] op_sel_hi:[0,1]
	v_cvt_pk_bf16_f32 v2, v2, v3
	v_cvt_pk_bf16_f32 v3, v4, v5
	v_pk_mul_f32 v[8:9], v[0:1], v[34:35] op_sel_hi:[0,1]
	v_cvt_pk_bf16_f32 v4, v10, v11
	v_cvt_pk_bf16_f32 v5, v8, v9
	v_mov_b64_e32 v[206:207], v[6:7]
	v_lshl_add_u64 v[210:211], v[6:7], 0, v[16:17]
	ds_write_b128 v21, v[2:5]
	s_mov_b64 s[4:5], -1
	v_pk_mul_f32 v[8:9], v[0:1], v[30:31] op_sel_hi:[0,1]
	v_pk_mul_f32 v[2:3], v[0:1], v[42:43] op_sel_hi:[0,1]
	v_pk_mul_f32 v[4:5], v[0:1], v[40:41] op_sel_hi:[0,1]
	v_pk_mul_f32 v[10:11], v[0:1], v[28:29] op_sel_hi:[0,1]
	v_cvt_pk_bf16_f32 v0, v4, v5
	v_cvt_pk_bf16_f32 v1, v2, v3
	v_cvt_pk_bf16_f32 v2, v10, v11
	v_cvt_pk_bf16_f32 v3, v8, v9
	s_waitcnt lgkmcnt(1)
	global_store_dwordx4 v[204:205], v[192:195], off
	global_store_dwordx4 v[208:209], v[196:199], off
	ds_write_b128 v21, v[0:3] offset:16
	ds_read_b128 v[192:195], v23
	ds_read_b128 v[196:199], v23 offset:1152
	s_waitcnt lgkmcnt(0)
	global_store_dwordx4 v[206:207], v[192:195], off
	global_store_dwordx4 v[210:211], v[196:199], off
	s_cbranch_vccnz .LBB0_203
	s_andn2_b64 vcc, exec, s[12:13]
	s_cbranch_vccnz .LBB0_202
	s_barrier
	s_branch .LBB0_202
